# attention: next item's Q fragments prefetched right after the K/V prefetch into dead VGPRs (not at item end)
# speedup vs baseline: 1.0076x; 1.0034x over previous
; __device__ __forceinline__ void attn_issue_q(const bf16* HB, const AttnItem& it, int tid, v4u (&qn)[4]) {
;     const int wave_ = tid >> 6, l15_ = tid & 15, g_ = (tid & 63) >> 4; const int qtok_ = it.tok0 + ((it.blk * 128 + wave_ * 16 + l15_) << it.dsh);
; #pragma unroll
;     for (int st = 0; st < 4; ++st) qn[st] = *(const v4u*)(HB + (size_t)qtok_ * 6144 + 3072 + it.hd * 128 + 8 * g_ + 32 * st);
; }
; __device__ __forceinline__ void ph_attn_mfma(const Frame& F) {
;     ...
;     if (ibase < iend) { const AttnItem it0 = attn_decode(ibase); attn_issue(HB, it0, tid, kreg, va, vb, false); attn_issue_q(HB, it0, tid, qn); }
.LBB0_858:
	s_or_b64 exec, exec, s[2:3]
	v_ashrrev_i32_e32 v0, 2, v86
	v_and_b32_e32 v0, -16, v0
	v_add_u32_e32 v0, s8, v0
	v_or_b32_e32 v0, v0, v84
	v_lshlrev_b32_e32 v0, s6, v0
	v_add_u32_e32 v0, s7, v0
	v_mov_b64_e32 v[52:53], s[10:11]
	s_movk_i32 s2, 0x3000
	v_mad_i64_i32 v[52:53], s[2:3], v0, s2, v[52:53]
	v_and_b32_e32 v0, 24, v56
	v_lshlrev_b32_e32 v0, 1, v0
	v_lshl_add_u64 v[52:53], v[52:53], 0, v[0:1]
	v_lshl_add_u64 v[2:3], v[2:3], 1, v[52:53]
	s_mov_b64 s[2:3], 0x1800
	v_lshl_add_u64 v[64:65], v[2:3], 0, s[2:3]
	v_add_co_u32_e32 v2, vcc, 0x1000, v2
	s_nop 1
	v_addc_co_u32_e32 v3, vcc, 0, v3, vcc
	global_load_dwordx4 v[212:215], v[64:65], off offset:64
	global_load_dwordx4 v[216:219], v[64:65], off offset:128
	global_load_dwordx4 v[220:223], v[2:3], off offset:2048
	s_nop 0
	global_load_dwordx4 v[224:227], v[64:65], off offset:192
	s_andn2_b64 vcc, exec, s[0:1]
	s_cbranch_vccnz .LBB0_831

; #define LAS __attribute__((address_space(3)))
; __device__ __forceinline__ void ph_attn_mfma(const Frame& F) {
;     ...
;         const AttnItem it = attn_decode(item);
;         const bool cont = havep && attn_cont(it, itp);
;         px = cont ? (px ^ 1) : 0;
;         itp = it; havep = true;
;         const int hd = it.hd, br = it.br, dsh = it.dsh, blk = it.blk, tok0 = it.tok0;
;         const int qtok = tok0 + ((blk * 128 + wave * 16 + l15) << dsh);
;         v4u qf[4];
; #pragma unroll
;         for (int st = 0; st < 4; ++st) qf[st] = qn[st];
;         __syncthreads();
; #pragma unroll
;         for (int i = 0; i < 8; ++i) { if (cont && i < 4) continue; const int c = tid + 512 * i, kj = (c >> 4) ^ (px << 7), ch = c & 15; *(LAS v4u*)(lds + AT_K_OFF + kj * AT_KROW + ch * 16) = kreg[i]; }
.LBB0_863:
	s_xor_b32 s2, s43, 1
	s_and_b64 vcc, s[18:19], exec
	s_cselect_b32 s43, s2, 0
	s_lshl_b32 s15, s43, 7
	s_waitcnt vmcnt(0) lgkmcnt(0)
	v_mov_b32_e32 v52, v212
	v_mov_b32_e32 v53, v213
	v_mov_b32_e32 v54, v214
	v_mov_b32_e32 v55, v215
	v_mov_b32_e32 v56, v216
	v_mov_b32_e32 v57, v217
	v_mov_b32_e32 v58, v218
	v_mov_b32_e32 v59, v219
	v_mov_b32_e32 v60, v220
	v_mov_b32_e32 v61, v221
	v_mov_b32_e32 v62, v222
	v_mov_b32_e32 v63, v223
	v_mov_b32_e32 v64, v224
	v_mov_b32_e32 v65, v225
	v_mov_b32_e32 v66, v226
	v_mov_b32_e32 v67, v227
	s_barrier
	s_cbranch_vccnz .LBB0_865
	v_xor_b32_e32 v0, s15, v121
	s_movk_i32 s4, 0x110
	v_mad_u64_u32 v[2:3], s[2:3], v0, s4, v[122:123]
	v_xor_b32_e32 v0, s15, v132
	ds_write_b128 v2, v[8:11]
	v_mad_u64_u32 v[2:3], s[2:3], v0, s4, v[122:123]
	v_xor_b32_e32 v0, s15, v134
	ds_write_b128 v2, v[4:7]
	v_mad_u64_u32 v[2:3], s[2:3], v0, s4, v[122:123]
	v_xor_b32_e32 v0, s15, v136
	ds_write_b128 v2, v[12:15]
	v_mad_u64_u32 v[2:3], s[2:3], v0, s4, v[122:123]
	ds_write_b128 v2, v[16:19]

; __device__ __forceinline__ void attn_issue_q(const bf16* HB, const AttnItem& it, int tid, v4u (&qn)[4]) {
;     const int wave_ = tid >> 6, l15_ = tid & 15, g_ = (tid & 63) >> 4; const int qtok_ = it.tok0 + ((it.blk * 128 + wave_ * 16 + l15_) << it.dsh);
; #pragma unroll
;     for (int st = 0; st < 4; ++st) qn[st] = *(const v4u*)(HB + (size_t)qtok_ * 6144 + 3072 + it.hd * 128 + 8 * g_ + 32 * st);
; }
; __device__ __forceinline__ void ph_attn_mfma(const Frame& F) {
;     ...
;         if (item + 1 < iend) { const AttnItem itn = attn_decode(item + 1); attn_issue(HB, itn, tid, kreg, va, vb, attn_cont(itn, it)); }
.LBB0_897:
	s_andn2_b64 vcc, exec, s[20:21]
	s_cbranch_vccnz .Lq_skip
	s_lshr_b32 s98, s40, 31
	s_ashr_i32 s99, s40, 6
	s_add_i32 s100, s99, s98
	s_mul_i32 s98, s100, 0xfffffe80
	s_add_i32 s98, s39, s98
	s_add_i32 s98, s98, 1
	s_ashr_i32 s99, s98, 6
	s_and_b32 s99, s99, -2
	s_lshr_b32 s101, 64, s99
	s_and_b32 s98, s98, 63
	s_sub_i32 m0, 6, s99
	s_add_i32 s101, s101, -1
	s_lshr_b32 m0, s98, m0
	s_and_b32 s98, s101, s98
	s_add_i32 s101, s36, 0x80
	s_and_b32 s101, s101, 0x2000
	v_lshl_add_u32 v228, s98, 7, v151
	s_or_b32 s101, m0, s101
	v_lshlrev_b32_e32 v228, s99, v228
	v_add_u32_e32 v228, s101, v228
	v_mov_b64_e32 v[230:231], s[10:11]
	s_movk_i32 s98, 0x3000
	v_mad_i64_i32 v[230:231], s[98:99], v228, s98, v[230:231]
	v_mov_b32_e32 v232, v130
	v_mov_b32_e32 v233, v1
	s_lshl_b32 s98, s100, 7
	v_lshl_add_u64 v[230:231], v[230:231], 0, v[232:233]
	s_ashr_i32 s99, s98, 31
	v_lshl_add_u64 v[230:231], s[98:99], 1, v[230:231]
	s_mov_b64 s[98:99], 0x1800
	v_lshl_add_u64 v[234:235], v[230:231], 0, s[98:99]
	v_add_co_u32_e32 v230, vcc, 0x1000, v230
	s_nop 1
	v_addc_co_u32_e32 v231, vcc, 0, v231, vcc
	global_load_dwordx4 v[212:215], v[234:235], off offset:64
	global_load_dwordx4 v[216:219], v[234:235], off offset:128
	global_load_dwordx4 v[220:223], v[230:231], off offset:2048
	s_nop 0
	global_load_dwordx4 v[224:227], v[234:235], off offset:192

; __device__ __forceinline__ void ph_attn_mfma(const Frame& F) {
;     ...
;         if (g == 0) LSE[((size_t)br * T + qtok) * 8 + hd] = mx * 0.6931471805599453f + __logf(sum);
;         if (item + 1 < iend) { const AttnItem itn = attn_decode(item + 1); attn_issue_q(HB, itn, tid, qn); }
;     }
.LBB0_899:
	s_or_b64 exec, exec, s[22:23]
	s_andn2_b64 vcc, exec, s[20:21]
	s_cbranch_vccnz .LBB0_860
	s_branch .LBB0_860
